# retention CUs: prep waves 4 and 5 (SIMD partners of the two scan waves) idle too; v29 otherwise
# baseline (speedup 1.0000x reference)
.LBB0_884:
	s_ashr_i32 s72, s8, 4
	s_ashr_i32 s73, s72, 31
	s_and_b32 s33, s8, 1
	s_lshl_b64 s[22:23], s[72:73], 12
	s_andn2_b64 vcc, exec, s[20:21]
	s_mov_b64 s[20:21], -1
	s_waitcnt lgkmcnt(0)
	s_barrier
	s_cbranch_vccnz .LBB0_957
	v_readlane_b32 s8, v254, 1
	v_readlane_b32 s9, v254, 2
	s_and_b64 vcc, exec, s[8:9]
	s_cbranch_vccz .LBB0_923
	v_readlane_b32 s8, v255, 8
	s_nop 3
	s_and_b32 s8, s8, 6
	s_cmp_eq_u32 s8, 4
	s_cbranch_scc1 .LBB0_879
	v_mov_b32_e32 v0, 0
	s_and_saveexec_b64 s[20:21], s[36:37]
	s_cbranch_execz .LBB0_890
	s_mov_b64 s[30:31], exec
	v_mbcnt_lo_u32_b32 v0, s30, 0
	v_mbcnt_hi_u32_b32 v0, s31, v0
	v_cmp_eq_u32_e32 vcc, 0, v0
	s_and_saveexec_b64 s[26:27], vcc
	s_cbranch_execz .LBB0_889
	s_bcnt1_i32_b64 s8, s[30:31]
	v_readlane_b32 s9, v255, 15
	v_mov_b32_e32 v2, s8
	s_nop 0
	v_mov_b32_e32 v1, s9
	ds_add_rtn_u32 v1, v1, v2
